# cached-block loads issued right behind the slot-table data wait (about 45 instructions earlier)
# speedup vs baseline: 1.0005x; 1.0005x over previous
.LBB3_6:
	s_xor_b32 s33, s32, 0xff
	s_add_i32 s33, s33, s24
	s_ashr_i32 s26, s33, 8
	v_cmp_gt_i32_e32 vcc, s24, v176
	v_med3_i32 v33, s26, 0, 6
	s_sub_i32 s33, s24, 0x100
	v_cmp_gt_i32_e64 s[4:5], s33, v176
	s_sub_i32 s33, s24, 0x200
	v_cmp_gt_i32_e64 s[6:7], s33, v176
	s_sub_i32 s33, s24, 0x300
	v_cmp_gt_i32_e64 s[8:9], s33, v176
	s_sub_i32 s33, s24, 0x400
	v_cmp_gt_i32_e64 s[10:11], s33, v176
	s_sub_i32 s33, s24, 0x500
	v_cmp_gt_i32_e64 s[12:13], s33, v176
	s_and_b32 s25, s25, 0x7ffff000
	s_mov_b32 s2, 0xffff0000
	v_readfirstlane_b32 s26, v33
	s_nop 3
	s_cmp_lt_i32 s26, 4
	s_waitcnt vmcnt(5)
	v_cndmask_b32_e32 v4, v29, v4, vcc
	v_cndmask_b32_e64 v134, v3, v2, s[0:1]
	v_cndmask_b32_e32 v134, 0, v134, vcc
	s_waitcnt vmcnt(4)
	v_cndmask_b32_e64 v3, v29, v8, s[4:5]
	v_cndmask_b32_e64 v97, v7, v6, s[0:1]
	v_cndmask_b32_e64 v97, 0, v97, s[4:5]
	v_cndmask_b32_e64 v135, 1.0, v4, s[0:1]
	v_cndmask_b32_e64 v33, -1, v9, s[4:5]
	v_cndmask_b32_e64 v98, 1.0, v3, s[0:1]
	s_waitcnt vmcnt(3)
	v_cndmask_b32_e64 v6, v29, v12, s[6:7]
	v_cndmask_b32_e64 v68, v11, v10, s[0:1]
	v_cndmask_b32_e64 v68, 0, v68, s[6:7]
	s_waitcnt vmcnt(2)
	v_cndmask_b32_e64 v7, v29, v16, s[8:9]
	v_cndmask_b32_e64 v70, 1.0, v6, s[0:1]
	v_cndmask_b32_e64 v73, 1.0, v7, s[0:1]
	v_cndmask_b32_e64 v34, -1, v13, s[6:7]
	v_cndmask_b32_e64 v35, -1, v17, s[8:9]
	v_cndmask_b32_e64 v71, v15, v14, s[0:1]
	v_cndmask_b32_e64 v71, 0, v71, s[8:9]
	s_waitcnt vmcnt(1)
	v_cndmask_b32_e64 v8, v29, v20, s[10:11]
	v_cndmask_b32_e64 v48, 1.0, v8, s[0:1]
	s_waitcnt vmcnt(0)
	s_cmpk_lt_i32 s24, 0x801
	s_cselect_b32 s47, 1, 0
	s_cbranch_scc0 .Lffc_nocache
	s_lshl_b32 s46, s27, 12
	s_add_u32 s46, s46, 0x8000
	s_add_u32 s44, s20, s46
	s_addc_u32 s45, s21, 0
	v_lshlrev_b32_e32 v183, 4, v38
	global_load_dwordx4 v[184:187], v183, s[44:45]
	global_load_dwordx4 v[188:191], v183, s[44:45] offset:1024
	global_load_dwordx4 v[192:195], v183, s[44:45] offset:2048
	global_load_dwordx4 v[196:199], v183, s[44:45] offset:3072
.Lffc_nocache:
	s_cmp_lt_i32 s26, 4
	v_cndmask_b32_e64 v10, v29, v24, s[12:13]
	v_cndmask_b32_e32 v29, -1, v5, vcc
	v_max_i32_e32 v4, 0, v29
	v_add_u32_e32 v4, s25, v4
	v_mov_b32_e32 v5, 0
	v_lshl_add_u64 v[6:7], v[4:5], 2, s[16:17]
	v_max_i32_e32 v4, 0, v33
	v_add_u32_e32 v4, s25, v4
	v_lshl_add_u64 v[8:9], v[4:5], 2, s[16:17]
	v_max_i32_e32 v4, 0, v34
	v_add_u32_e32 v4, s25, v4
	v_cndmask_b32_e64 v3, 1.0, v10, s[0:1]
	v_lshl_add_u64 v[10:11], v[4:5], 2, s[16:17]
	v_max_i32_e32 v4, 0, v35
	v_cndmask_b32_e64 v36, -1, v21, s[10:11]
	v_add_u32_e32 v4, s25, v4
	v_lshl_add_u64 v[12:13], v[4:5], 2, s[16:17]
	v_max_i32_e32 v4, 0, v36
	v_cndmask_b32_e64 v37, -1, v25, s[12:13]
	v_add_u32_e32 v4, s25, v4
	v_lshl_add_u64 v[14:15], v[4:5], 2, s[16:17]
	v_max_i32_e32 v4, 0, v37
	v_cndmask_b32_e64 v46, v19, v18, s[0:1]
	v_cndmask_b32_e64 v46, 0, v46, s[10:11]
	v_cndmask_b32_e64 v2, v23, v22, s[0:1]
	v_cndmask_b32_e64 v2, 0, v2, s[12:13]
	v_add_u32_e32 v4, s25, v4
	v_lshl_add_u64 v[4:5], v[4:5], 2, s[16:17]
	global_load_dword v133, v[6:7], off
	global_load_dword v132, v[8:9], off
	global_load_dword v131, v[10:11], off
	global_load_dword v130, v[12:13], off
	global_load_dword v129, v[14:15], off
	global_load_dword v128, v[4:5], off
	v_max_f32_e32 v6, v32, v32
	v_cndmask_b32_e64 v4, v31, v30, s[0:1]
	v_max_f32_e32 v6, 0xc6ea6000, v6
	v_cndmask_b32_e64 v6, v6, 1.0, s[0:1]
	v_and_b32_e32 v7, 0xffff0000, v4
	v_sub_f32_e32 v8, v4, v7
	v_or_b32_sdwa v22, v4, v7 dst_sel:DWORD dst_unused:UNUSED_PAD src0_sel:WORD_1 src1_sel:DWORD
	v_and_b32_e32 v4, 0xffff0000, v6
	v_sub_f32_e32 v7, v6, v4
	v_or_b32_sdwa v24, v6, v4 dst_sel:DWORD dst_unused:UNUSED_PAD src0_sel:WORD_1 src1_sel:DWORD
	v_or_b32_sdwa v23, v8, v4 dst_sel:DWORD dst_unused:UNUSED_PAD src0_sel:WORD_1 src1_sel:DWORD
	v_max_f32_e32 v4, v28, v28
	v_cndmask_b32_e64 v5, v27, v26, s[0:1]
	v_and_b32_e32 v9, 0xffff0000, v7
	v_max_f32_e32 v4, 0xc6ea6000, v4
	v_sub_f32_e32 v9, v7, v9
	v_lshrrev_b32_e32 v7, 16, v7
	v_cndmask_b32_e64 v4, v4, 1.0, s[0:1]
	v_and_b32_e32 v6, 0xffff0000, v5
	v_and_or_b32 v25, v9, s2, v7
	v_sub_f32_e32 v7, v5, v6
	v_or_b32_sdwa v18, v5, v6 dst_sel:DWORD dst_unused:UNUSED_PAD src0_sel:WORD_1 src1_sel:DWORD
	v_and_b32_e32 v5, 0xffff0000, v4
	v_sub_f32_e32 v6, v4, v5
	v_and_b32_e32 v8, 0xffff0000, v6
	v_sub_f32_e32 v8, v6, v8
	v_lshrrev_b32_e32 v6, 16, v6
	v_or_b32_sdwa v20, v4, v5 dst_sel:DWORD dst_unused:UNUSED_PAD src0_sel:WORD_1 src1_sel:DWORD
	v_or_b32_sdwa v19, v7, v5 dst_sel:DWORD dst_unused:UNUSED_PAD src0_sel:WORD_1 src1_sel:DWORD
	v_and_or_b32 v21, v8, s2, v6
	s_mov_b64 s[2:3], 0
	s_cbranch_scc1 .LBB3_11
	s_cmp_gt_i32 s26, 4
	s_cbranch_scc0 .LBB3_14
	s_cmp_gt_i32 s26, 5
	s_cbranch_scc0 .LBB3_15
	s_cmp_eq_u32 s26, 6
	s_mov_b64 s[4:5], 0
	s_cbranch_scc0 .LBB3_48
	v_and_b32_e32 v4, 0xffff0000, v2
	v_max_f32_e32 v3, v3, v3
	v_sub_f32_e32 v4, v2, v4
	v_max_f32_e32 v3, 0xc6ea6000, v3
	v_and_b32_e32 v5, 0xffff0000, v3
	v_and_b32_e32 v4, 0xffff0000, v4
	v_or_b32_sdwa v75, v5, v2 dst_sel:DWORD dst_unused:UNUSED_PAD src0_sel:DWORD src1_sel:WORD_1
	v_or_b32_sdwa v74, v4, v2 dst_sel:DWORD dst_unused:UNUSED_PAD src0_sel:DWORD src1_sel:WORD_1
	v_sub_f32_e32 v2, v3, v5
	v_and_b32_e32 v4, 0xffff0000, v2
	s_mov_b32 s6, 0xffff0000
	v_sub_f32_e32 v4, v2, v4
	v_lshrrev_b32_e32 v2, 16, v2
	v_and_or_b32 v76, v4, s6, v2
	v_or_b32_sdwa v77, v3, v5 dst_sel:DWORD dst_unused:UNUSED_PAD src0_sel:WORD_1 src1_sel:DWORD
	s_movk_i32 s6, 0xfc00
	s_mov_b64 s[8:9], -1
	v_mfma_f32_32x32x16_bf16 v[2:17], v[22:25], v[74:77], 0
	s_nop 11
	v_cvt_pk_f16_f32 v2, v2, v3
	v_cvt_pk_f16_f32 v3, v4, v5
	v_pk_max_i16 v2, v2, s6 op_sel_hi:[1,0]
	v_pk_max_i16 v3, v3, s6 op_sel_hi:[1,0]
	s_nop 0
	v_exp_f16_e32 v43, v2
	v_exp_f16_e32 v45, v3
	v_exp_f16_sdwa v43, v2 dst_sel:WORD_1 dst_unused:UNUSED_PRESERVE src0_sel:WORD_1
	v_exp_f16_sdwa v45, v3 dst_sel:WORD_1 dst_unused:UNUSED_PRESERVE src0_sel:WORD_1
	v_cvt_pk_f16_f32 v2, v6, v7
	v_cvt_pk_f16_f32 v3, v8, v9
	v_pk_max_i16 v2, v2, s6 op_sel_hi:[1,0]
	v_pk_max_i16 v3, v3, s6 op_sel_hi:[1,0]
	s_nop 0
	v_exp_f16_e32 v50, v2
	v_exp_f16_e32 v54, v3
	v_exp_f16_sdwa v50, v2 dst_sel:WORD_1 dst_unused:UNUSED_PRESERVE src0_sel:WORD_1
	v_exp_f16_sdwa v54, v3 dst_sel:WORD_1 dst_unused:UNUSED_PRESERVE src0_sel:WORD_1
	v_cvt_pk_f16_f32 v2, v10, v11
	v_cvt_pk_f16_f32 v3, v12, v13
	v_pk_max_i16 v2, v2, s6 op_sel_hi:[1,0]
	v_pk_max_i16 v3, v3, s6 op_sel_hi:[1,0]
	s_nop 0
	v_exp_f16_e32 v58, v2
	v_exp_f16_e32 v61, v3
	v_exp_f16_sdwa v58, v2 dst_sel:WORD_1 dst_unused:UNUSED_PRESERVE src0_sel:WORD_1
	v_exp_f16_sdwa v61, v3 dst_sel:WORD_1 dst_unused:UNUSED_PRESERVE src0_sel:WORD_1
	v_cvt_pk_f16_f32 v2, v14, v15
	v_cvt_pk_f16_f32 v3, v16, v17
	v_pk_max_i16 v2, v2, s6 op_sel_hi:[1,0]
	v_pk_max_i16 v3, v3, s6 op_sel_hi:[1,0]
	s_nop 0
	v_exp_f16_e32 v64, v2
	v_exp_f16_e32 v66, v3
	v_exp_f16_sdwa v64, v2 dst_sel:WORD_1 dst_unused:UNUSED_PRESERVE src0_sel:WORD_1
	v_exp_f16_sdwa v66, v3 dst_sel:WORD_1 dst_unused:UNUSED_PRESERVE src0_sel:WORD_1
	v_mfma_f32_32x32x16_bf16 v[2:17], v[18:21], v[74:77], 0
	s_nop 11
	v_cvt_pk_f16_f32 v2, v2, v3
	v_cvt_pk_f16_f32 v3, v4, v5
	v_pk_max_i16 v2, v2, s6 op_sel_hi:[1,0]
	v_pk_max_i16 v3, v3, s6 op_sel_hi:[1,0]
	s_nop 0
	v_exp_f16_e32 v72, v2
	v_exp_f16_e32 v76, v3
	v_exp_f16_sdwa v72, v2 dst_sel:WORD_1 dst_unused:UNUSED_PRESERVE src0_sel:WORD_1
	v_exp_f16_sdwa v76, v3 dst_sel:WORD_1 dst_unused:UNUSED_PRESERVE src0_sel:WORD_1
	v_cvt_pk_f16_f32 v2, v6, v7
	v_cvt_pk_f16_f32 v3, v8, v9
	v_pk_max_i16 v2, v2, s6 op_sel_hi:[1,0]
	v_pk_max_i16 v3, v3, s6 op_sel_hi:[1,0]
	s_nop 0
	v_exp_f16_e32 v83, v2
	v_exp_f16_e32 v85, v3
	v_exp_f16_sdwa v83, v2 dst_sel:WORD_1 dst_unused:UNUSED_PRESERVE src0_sel:WORD_1
	v_exp_f16_sdwa v85, v3 dst_sel:WORD_1 dst_unused:UNUSED_PRESERVE src0_sel:WORD_1
	v_cvt_pk_f16_f32 v2, v10, v11
	v_cvt_pk_f16_f32 v3, v12, v13
	v_pk_max_i16 v2, v2, s6 op_sel_hi:[1,0]
	v_pk_max_i16 v3, v3, s6 op_sel_hi:[1,0]
	s_nop 0
	v_exp_f16_e32 v89, v2
	v_exp_f16_e32 v92, v3
	v_exp_f16_sdwa v89, v2 dst_sel:WORD_1 dst_unused:UNUSED_PRESERVE src0_sel:WORD_1
	v_exp_f16_sdwa v92, v3 dst_sel:WORD_1 dst_unused:UNUSED_PRESERVE src0_sel:WORD_1
	v_cvt_pk_f16_f32 v2, v14, v15
	v_cvt_pk_f16_f32 v3, v16, v17
	v_pk_max_i16 v2, v2, s6 op_sel_hi:[1,0]
	v_pk_max_i16 v3, v3, s6 op_sel_hi:[1,0]
	s_nop 0
	v_exp_f16_e32 v95, v2
	v_exp_f16_e32 v96, v3
	v_exp_f16_sdwa v95, v2 dst_sel:WORD_1 dst_unused:UNUSED_PRESERVE src0_sel:WORD_1
	v_exp_f16_sdwa v96, v3 dst_sel:WORD_1 dst_unused:UNUSED_PRESERVE src0_sel:WORD_1
	s_and_b64 vcc, exec, s[4:5]
	s_cbranch_vccnz .LBB3_16
	s_branch .LBB3_17

.LBB4_6:
	s_xor_b32 s33, s32, 0xff
	s_add_i32 s33, s33, s26
	s_ashr_i32 s27, s33, 8
	v_cmp_gt_i32_e32 vcc, s26, v176
	v_med3_i32 v33, s27, 0, 6
	s_sub_i32 s33, s26, 0x100
	v_cmp_gt_i32_e64 s[4:5], s33, v176
	s_sub_i32 s33, s26, 0x200
	v_cmp_gt_i32_e64 s[6:7], s33, v176
	s_sub_i32 s33, s26, 0x300
	v_cmp_gt_i32_e64 s[8:9], s33, v176
	s_sub_i32 s33, s26, 0x400
	v_cmp_gt_i32_e64 s[10:11], s33, v176
	s_sub_i32 s33, s26, 0x500
	v_cmp_gt_i32_e64 s[12:13], s33, v176
	s_and_b32 s27, s29, 0x7ffff000
	s_mov_b32 s2, 0xffff0000
	v_readfirstlane_b32 s28, v33
	s_nop 3
	s_cmp_lt_i32 s28, 4
	s_waitcnt vmcnt(5)
	v_cndmask_b32_e32 v4, v29, v4, vcc
	v_cndmask_b32_e64 v134, v3, v2, s[0:1]
	v_cndmask_b32_e32 v134, 0, v134, vcc
	s_waitcnt vmcnt(4)
	v_cndmask_b32_e64 v3, v29, v8, s[4:5]
	v_cndmask_b32_e64 v97, v7, v6, s[0:1]
	v_cndmask_b32_e64 v97, 0, v97, s[4:5]
	v_cndmask_b32_e64 v135, 1.0, v4, s[0:1]
	v_cndmask_b32_e64 v33, -1, v9, s[4:5]
	v_cndmask_b32_e64 v98, 1.0, v3, s[0:1]
	s_waitcnt vmcnt(3)
	v_cndmask_b32_e64 v6, v29, v12, s[6:7]
	v_cndmask_b32_e64 v68, v11, v10, s[0:1]
	v_cndmask_b32_e64 v68, 0, v68, s[6:7]
	s_waitcnt vmcnt(2)
	v_cndmask_b32_e64 v7, v29, v16, s[8:9]
	v_cndmask_b32_e64 v70, 1.0, v6, s[0:1]
	v_cndmask_b32_e64 v73, 1.0, v7, s[0:1]
	v_cndmask_b32_e64 v34, -1, v13, s[6:7]
	v_cndmask_b32_e64 v35, -1, v17, s[8:9]
	v_cndmask_b32_e64 v71, v15, v14, s[0:1]
	v_cndmask_b32_e64 v71, 0, v71, s[8:9]
	s_waitcnt vmcnt(1)
	v_cndmask_b32_e64 v8, v29, v20, s[10:11]
	v_cndmask_b32_e64 v48, 1.0, v8, s[0:1]
	s_waitcnt vmcnt(0)
	s_cmpk_lt_i32 s26, 0x801
	s_cselect_b32 s47, 1, 0
	s_cbranch_scc0 .Lftc_nocache
	s_lshl_b32 s46, s30, 12
	s_add_u32 s46, s46, 0x8000
	s_add_u32 s44, s20, s46
	s_addc_u32 s45, s21, 0
	v_lshlrev_b32_e32 v183, 4, v38
	global_load_dwordx4 v[184:187], v183, s[44:45]
	global_load_dwordx4 v[188:191], v183, s[44:45] offset:1024
	global_load_dwordx4 v[192:195], v183, s[44:45] offset:2048
	global_load_dwordx4 v[196:199], v183, s[44:45] offset:3072
.Lftc_nocache:
	s_cmp_lt_i32 s28, 4
	v_cndmask_b32_e64 v10, v29, v24, s[12:13]
	v_cndmask_b32_e32 v29, -1, v5, vcc
	v_max_i32_e32 v4, 0, v29
	v_add_u32_e32 v4, s27, v4
	v_mov_b32_e32 v5, 0
	v_lshl_add_u64 v[6:7], v[4:5], 2, s[16:17]
	v_max_i32_e32 v4, 0, v33
	v_add_u32_e32 v4, s27, v4
	v_lshl_add_u64 v[8:9], v[4:5], 2, s[16:17]
	v_max_i32_e32 v4, 0, v34
	v_add_u32_e32 v4, s27, v4
	v_cndmask_b32_e64 v3, 1.0, v10, s[0:1]
	v_lshl_add_u64 v[10:11], v[4:5], 2, s[16:17]
	v_max_i32_e32 v4, 0, v35
	v_cndmask_b32_e64 v36, -1, v21, s[10:11]
	v_add_u32_e32 v4, s27, v4
	v_lshl_add_u64 v[12:13], v[4:5], 2, s[16:17]
	v_max_i32_e32 v4, 0, v36
	v_cndmask_b32_e64 v37, -1, v25, s[12:13]
	v_add_u32_e32 v4, s27, v4
	v_lshl_add_u64 v[14:15], v[4:5], 2, s[16:17]
	v_max_i32_e32 v4, 0, v37
	v_cndmask_b32_e64 v46, v19, v18, s[0:1]
	v_cndmask_b32_e64 v46, 0, v46, s[10:11]
	v_cndmask_b32_e64 v2, v23, v22, s[0:1]
	v_cndmask_b32_e64 v2, 0, v2, s[12:13]
	v_add_u32_e32 v4, s27, v4
	v_lshl_add_u64 v[4:5], v[4:5], 2, s[16:17]
	global_load_dword v133, v[6:7], off
	global_load_dword v132, v[8:9], off
	global_load_dword v131, v[10:11], off
	global_load_dword v130, v[12:13], off
	global_load_dword v129, v[14:15], off
	global_load_dword v128, v[4:5], off
	v_max_f32_e32 v6, v32, v32
	v_cndmask_b32_e64 v4, v31, v30, s[0:1]
	v_max_f32_e32 v6, 0xc6ea6000, v6
	v_cndmask_b32_e64 v6, v6, 1.0, s[0:1]
	v_and_b32_e32 v7, 0xffff0000, v4
	v_sub_f32_e32 v8, v4, v7
	v_or_b32_sdwa v22, v4, v7 dst_sel:DWORD dst_unused:UNUSED_PAD src0_sel:WORD_1 src1_sel:DWORD
	v_and_b32_e32 v4, 0xffff0000, v6
	v_sub_f32_e32 v7, v6, v4
	v_or_b32_sdwa v24, v6, v4 dst_sel:DWORD dst_unused:UNUSED_PAD src0_sel:WORD_1 src1_sel:DWORD
	v_or_b32_sdwa v23, v8, v4 dst_sel:DWORD dst_unused:UNUSED_PAD src0_sel:WORD_1 src1_sel:DWORD
	v_max_f32_e32 v4, v28, v28
	v_cndmask_b32_e64 v5, v27, v26, s[0:1]
	v_and_b32_e32 v9, 0xffff0000, v7
	v_max_f32_e32 v4, 0xc6ea6000, v4
	v_sub_f32_e32 v9, v7, v9
	v_lshrrev_b32_e32 v7, 16, v7
	v_cndmask_b32_e64 v4, v4, 1.0, s[0:1]
	v_and_b32_e32 v6, 0xffff0000, v5
	v_and_or_b32 v25, v9, s2, v7
	v_sub_f32_e32 v7, v5, v6
	v_or_b32_sdwa v18, v5, v6 dst_sel:DWORD dst_unused:UNUSED_PAD src0_sel:WORD_1 src1_sel:DWORD
	v_and_b32_e32 v5, 0xffff0000, v4
	v_sub_f32_e32 v6, v4, v5
	v_and_b32_e32 v8, 0xffff0000, v6
	v_sub_f32_e32 v8, v6, v8
	v_lshrrev_b32_e32 v6, 16, v6
	v_or_b32_sdwa v20, v4, v5 dst_sel:DWORD dst_unused:UNUSED_PAD src0_sel:WORD_1 src1_sel:DWORD
	v_or_b32_sdwa v19, v7, v5 dst_sel:DWORD dst_unused:UNUSED_PAD src0_sel:WORD_1 src1_sel:DWORD
	v_and_or_b32 v21, v8, s2, v6
	s_mov_b64 s[2:3], 0
	s_cbranch_scc1 .LBB4_11
	s_cmp_gt_i32 s28, 4
	s_cbranch_scc0 .LBB4_14
	s_cmp_gt_i32 s28, 5
	s_cbranch_scc0 .LBB4_15
	s_cmp_eq_u32 s28, 6
	s_mov_b64 s[4:5], 0
	s_cbranch_scc0 .LBB4_48
	v_and_b32_e32 v4, 0xffff0000, v2
	v_max_f32_e32 v3, v3, v3
	v_sub_f32_e32 v4, v2, v4
	v_max_f32_e32 v3, 0xc6ea6000, v3
	v_and_b32_e32 v5, 0xffff0000, v3
	v_and_b32_e32 v4, 0xffff0000, v4
	v_or_b32_sdwa v75, v5, v2 dst_sel:DWORD dst_unused:UNUSED_PAD src0_sel:DWORD src1_sel:WORD_1
	v_or_b32_sdwa v74, v4, v2 dst_sel:DWORD dst_unused:UNUSED_PAD src0_sel:DWORD src1_sel:WORD_1
	v_sub_f32_e32 v2, v3, v5
	v_and_b32_e32 v4, 0xffff0000, v2
	s_mov_b32 s6, 0xffff0000
	v_sub_f32_e32 v4, v2, v4
	v_lshrrev_b32_e32 v2, 16, v2
	v_and_or_b32 v76, v4, s6, v2
	v_or_b32_sdwa v77, v3, v5 dst_sel:DWORD dst_unused:UNUSED_PAD src0_sel:WORD_1 src1_sel:DWORD
	s_movk_i32 s6, 0xfc00
	s_mov_b64 s[8:9], -1
	v_mfma_f32_32x32x16_bf16 v[2:17], v[22:25], v[74:77], 0
	s_nop 11
	v_cvt_pk_f16_f32 v2, v2, v3
	v_cvt_pk_f16_f32 v3, v4, v5
	v_pk_max_i16 v2, v2, s6 op_sel_hi:[1,0]
	v_pk_max_i16 v3, v3, s6 op_sel_hi:[1,0]
	s_nop 0
	v_exp_f16_e32 v43, v2
	v_exp_f16_e32 v45, v3
	v_exp_f16_sdwa v43, v2 dst_sel:WORD_1 dst_unused:UNUSED_PRESERVE src0_sel:WORD_1
	v_exp_f16_sdwa v45, v3 dst_sel:WORD_1 dst_unused:UNUSED_PRESERVE src0_sel:WORD_1
	v_cvt_pk_f16_f32 v2, v6, v7
	v_cvt_pk_f16_f32 v3, v8, v9
	v_pk_max_i16 v2, v2, s6 op_sel_hi:[1,0]
	v_pk_max_i16 v3, v3, s6 op_sel_hi:[1,0]
	s_nop 0
	v_exp_f16_e32 v50, v2
	v_exp_f16_e32 v54, v3
	v_exp_f16_sdwa v50, v2 dst_sel:WORD_1 dst_unused:UNUSED_PRESERVE src0_sel:WORD_1
	v_exp_f16_sdwa v54, v3 dst_sel:WORD_1 dst_unused:UNUSED_PRESERVE src0_sel:WORD_1
	v_cvt_pk_f16_f32 v2, v10, v11
	v_cvt_pk_f16_f32 v3, v12, v13
	v_pk_max_i16 v2, v2, s6 op_sel_hi:[1,0]
	v_pk_max_i16 v3, v3, s6 op_sel_hi:[1,0]
	s_nop 0
	v_exp_f16_e32 v58, v2
	v_exp_f16_e32 v61, v3
	v_exp_f16_sdwa v58, v2 dst_sel:WORD_1 dst_unused:UNUSED_PRESERVE src0_sel:WORD_1
	v_exp_f16_sdwa v61, v3 dst_sel:WORD_1 dst_unused:UNUSED_PRESERVE src0_sel:WORD_1
	v_cvt_pk_f16_f32 v2, v14, v15
	v_cvt_pk_f16_f32 v3, v16, v17
	v_pk_max_i16 v2, v2, s6 op_sel_hi:[1,0]
	v_pk_max_i16 v3, v3, s6 op_sel_hi:[1,0]
	s_nop 0
	v_exp_f16_e32 v64, v2
	v_exp_f16_e32 v66, v3
	v_exp_f16_sdwa v64, v2 dst_sel:WORD_1 dst_unused:UNUSED_PRESERVE src0_sel:WORD_1
	v_exp_f16_sdwa v66, v3 dst_sel:WORD_1 dst_unused:UNUSED_PRESERVE src0_sel:WORD_1
	v_mfma_f32_32x32x16_bf16 v[2:17], v[18:21], v[74:77], 0
	s_nop 11
	v_cvt_pk_f16_f32 v2, v2, v3
	v_cvt_pk_f16_f32 v3, v4, v5
	v_pk_max_i16 v2, v2, s6 op_sel_hi:[1,0]
	v_pk_max_i16 v3, v3, s6 op_sel_hi:[1,0]
	s_nop 0
	v_exp_f16_e32 v72, v2
	v_exp_f16_e32 v76, v3
	v_exp_f16_sdwa v72, v2 dst_sel:WORD_1 dst_unused:UNUSED_PRESERVE src0_sel:WORD_1
	v_exp_f16_sdwa v76, v3 dst_sel:WORD_1 dst_unused:UNUSED_PRESERVE src0_sel:WORD_1
	v_cvt_pk_f16_f32 v2, v6, v7
	v_cvt_pk_f16_f32 v3, v8, v9
	v_pk_max_i16 v2, v2, s6 op_sel_hi:[1,0]
	v_pk_max_i16 v3, v3, s6 op_sel_hi:[1,0]
	s_nop 0
	v_exp_f16_e32 v83, v2
	v_exp_f16_e32 v85, v3
	v_exp_f16_sdwa v83, v2 dst_sel:WORD_1 dst_unused:UNUSED_PRESERVE src0_sel:WORD_1
	v_exp_f16_sdwa v85, v3 dst_sel:WORD_1 dst_unused:UNUSED_PRESERVE src0_sel:WORD_1
	v_cvt_pk_f16_f32 v2, v10, v11
	v_cvt_pk_f16_f32 v3, v12, v13
	v_pk_max_i16 v2, v2, s6 op_sel_hi:[1,0]
	v_pk_max_i16 v3, v3, s6 op_sel_hi:[1,0]
	s_nop 0
	v_exp_f16_e32 v89, v2
	v_exp_f16_e32 v92, v3
	v_exp_f16_sdwa v89, v2 dst_sel:WORD_1 dst_unused:UNUSED_PRESERVE src0_sel:WORD_1
	v_exp_f16_sdwa v92, v3 dst_sel:WORD_1 dst_unused:UNUSED_PRESERVE src0_sel:WORD_1
	v_cvt_pk_f16_f32 v2, v14, v15
	v_cvt_pk_f16_f32 v3, v16, v17
	v_pk_max_i16 v2, v2, s6 op_sel_hi:[1,0]
	v_pk_max_i16 v3, v3, s6 op_sel_hi:[1,0]
	s_nop 0
	v_exp_f16_e32 v95, v2
	v_exp_f16_e32 v96, v3
	v_exp_f16_sdwa v95, v2 dst_sel:WORD_1 dst_unused:UNUSED_PRESERVE src0_sel:WORD_1
	v_exp_f16_sdwa v96, v3 dst_sel:WORD_1 dst_unused:UNUSED_PRESERVE src0_sel:WORD_1
	s_and_b64 vcc, exec, s[4:5]
	s_cbranch_vccnz .LBB4_16
	s_branch .LBB4_17
